# pools repartition (P832/DU832 q7/4112/4112) + adaLN 2x unroll (re-measure)
# speedup vs baseline: 1.0100x; 1.0025x over previous
.LBB0_21:
	v_add_co_u32_e32 v44, vcc, 0xc000, v34
	s_mov_b64 s[0:1], vcc
	v_add_co_u32_e32 v48, vcc, 0x18000, v34
	s_mov_b64 s[2:3], vcc
	v_addc_co_u32_e64 v45, vcc, 0, v35, s[0:1]
	v_add_co_u32_e32 v52, vcc, 0x24000, v34
	s_mov_b64 s[0:1], vcc
	v_addc_co_u32_e64 v49, vcc, 0, v35, s[2:3]
	v_add_co_u32_e32 v56, vcc, 0x30000, v34
	s_mov_b64 s[2:3], vcc
	v_addc_co_u32_e64 v53, vcc, 0, v35, s[0:1]
	v_add_co_u32_e32 v60, vcc, 0x3c000, v34
	s_mov_b64 s[0:1], vcc
	v_addc_co_u32_e64 v57, vcc, 0, v35, s[2:3]
	v_add_co_u32_e32 v64, vcc, 0x48000, v34
	s_mov_b64 s[2:3], vcc
	v_addc_co_u32_e64 v61, vcc, 0, v35, s[0:1]
	v_add_co_u32_e32 v68, vcc, 0x54000, v34
	s_mov_b64 s[0:1], vcc
	v_addc_co_u32_e64 v65, vcc, 0, v35, s[2:3]
	v_add_co_u32_e32 v72, vcc, 0x60000, v34
	global_load_dwordx4 v[10:13], v[34:35], off
	s_mov_b64 s[2:3], vcc
	v_addc_co_u32_e64 v69, vcc, 0, v35, s[0:1]
	ds_read_b128 v[18:21], v39
	ds_read_b128 v[14:17], v39 offset:16
	ds_read_b128 v[22:25], v39 offset:8192
	ds_read_b128 v[40:43], v39 offset:8208
	global_load_dwordx4 v[44:47], v[44:45], off
	v_add_co_u32_e32 v76, vcc, 0x6c000, v34
	global_load_dwordx4 v[48:51], v[48:49], off
	s_mov_b64 s[0:1], vcc
	v_addc_co_u32_e64 v73, vcc, 0, v35, s[2:3]
	global_load_dwordx4 v[52:55], v[52:53], off
	v_add_co_u32_e32 v80, vcc, 0x78000, v34
	global_load_dwordx4 v[56:59], v[56:57], off
	s_mov_b64 s[2:3], vcc
	v_addc_co_u32_e64 v77, vcc, 0, v35, s[0:1]
	global_load_dwordx4 v[60:63], v[60:61], off
	v_add_co_u32_e32 v84, vcc, 0x84000, v34
	global_load_dwordx4 v[64:67], v[64:65], off
	s_mov_b64 s[0:1], vcc
	v_addc_co_u32_e64 v81, vcc, 0, v35, s[2:3]
	global_load_dwordx4 v[68:71], v[68:69], off
	v_add_co_u32_e32 v88, vcc, 0x90000, v34
	global_load_dwordx4 v[72:75], v[72:73], off
	s_mov_b64 s[2:3], vcc
	v_addc_co_u32_e64 v85, vcc, 0, v35, s[0:1]
	global_load_dwordx4 v[76:79], v[76:77], off
	v_add_co_u32_e32 v92, vcc, 0x9c000, v34
	global_load_dwordx4 v[80:83], v[80:81], off
	s_mov_b64 s[0:1], vcc
	v_addc_co_u32_e64 v89, vcc, 0, v35, s[2:3]
	global_load_dwordx4 v[84:87], v[84:85], off
	v_add_co_u32_e32 v96, vcc, 0xa8000, v34
	s_mov_b64 s[2:3], vcc
	global_load_dwordx4 v[88:91], v[88:89], off
	v_addc_co_u32_e64 v93, vcc, 0, v35, s[0:1]
	global_load_dwordx4 v[92:95], v[92:93], off
	v_add_co_u32_e32 v100, vcc, 0xb4000, v34
	v_addc_co_u32_e64 v97, s[0:1], 0, v35, s[2:3]
	global_load_dwordx4 v[96:99], v[96:97], off
	v_addc_co_u32_e32 v101, vcc, 0, v35, vcc
	global_load_dwordx4 v[100:103], v[100:101], off
	s_waitcnt lgkmcnt(3)
	v_mov_b32_e32 v120, v21
	s_waitcnt lgkmcnt(1)
	v_mov_b32_e32 v122, v25
	ds_read_b128 v[104:107], v39 offset:32
	ds_read_b128 v[108:111], v39 offset:48
	ds_read_b128 v[112:115], v39 offset:8224
	ds_read_b128 v[116:119], v39 offset:8240
	v_mov_b32_e32 v124, v17
	s_waitcnt lgkmcnt(4)
	v_mov_b32_e32 v126, v43
	s_waitcnt lgkmcnt(3)
	v_mov_b32_e32 v128, v107
	s_waitcnt lgkmcnt(1)
	v_mov_b32_e32 v130, v115
	v_mov_b32_e32 v132, v111
	s_waitcnt lgkmcnt(0)
	v_mov_b32_e32 v134, v119
	v_add_u32_e32 v39, 64, v39
	v_lshl_add_u64 v[34:35], v[34:35], 0, s[4:5]
	v_add_co_u32_e32 v140, vcc, 0xc000, v34
	s_mov_b64 s[0:1], vcc
	v_add_co_u32_e32 v144, vcc, 0x18000, v34
	s_mov_b64 s[2:3], vcc
	v_addc_co_u32_e64 v141, vcc, 0, v35, s[0:1]
	v_add_co_u32_e32 v148, vcc, 0x24000, v34
	s_mov_b64 s[0:1], vcc
	v_addc_co_u32_e64 v145, vcc, 0, v35, s[2:3]
	v_add_co_u32_e32 v152, vcc, 0x30000, v34
	s_mov_b64 s[2:3], vcc
	v_addc_co_u32_e64 v149, vcc, 0, v35, s[0:1]
	v_add_co_u32_e32 v156, vcc, 0x3c000, v34
	s_mov_b64 s[0:1], vcc
	v_addc_co_u32_e64 v153, vcc, 0, v35, s[2:3]
	v_add_co_u32_e32 v160, vcc, 0x48000, v34
	s_mov_b64 s[2:3], vcc
	v_addc_co_u32_e64 v157, vcc, 0, v35, s[0:1]
	v_add_co_u32_e32 v164, vcc, 0x54000, v34
	s_mov_b64 s[0:1], vcc
	v_addc_co_u32_e64 v161, vcc, 0, v35, s[2:3]
	v_add_co_u32_e32 v168, vcc, 0x60000, v34
	global_load_dwordx4 v[136:139], v[34:35], off
	s_mov_b64 s[2:3], vcc
	v_addc_co_u32_e64 v165, vcc, 0, v35, s[0:1]
	ds_read_b128 v[204:207], v39
	ds_read_b128 v[200:203], v39 offset:16
	ds_read_b128 v[208:211], v39 offset:8192
	ds_read_b128 v[212:215], v39 offset:8208
	global_load_dwordx4 v[140:143], v[140:141], off
	v_add_co_u32_e32 v172, vcc, 0x6c000, v34
	global_load_dwordx4 v[144:147], v[144:145], off
	s_mov_b64 s[0:1], vcc
	v_addc_co_u32_e64 v169, vcc, 0, v35, s[2:3]
	global_load_dwordx4 v[148:151], v[148:149], off
	v_add_co_u32_e32 v176, vcc, 0x78000, v34
	global_load_dwordx4 v[152:155], v[152:153], off
	s_mov_b64 s[2:3], vcc
	v_addc_co_u32_e64 v173, vcc, 0, v35, s[0:1]
	global_load_dwordx4 v[156:159], v[156:157], off
	v_add_co_u32_e32 v180, vcc, 0x84000, v34
	global_load_dwordx4 v[160:163], v[160:161], off
	s_mov_b64 s[0:1], vcc
	v_addc_co_u32_e64 v177, vcc, 0, v35, s[2:3]
	global_load_dwordx4 v[164:167], v[164:165], off
	v_add_co_u32_e32 v184, vcc, 0x90000, v34
	global_load_dwordx4 v[168:171], v[168:169], off
	s_mov_b64 s[2:3], vcc
	v_addc_co_u32_e64 v181, vcc, 0, v35, s[0:1]
	global_load_dwordx4 v[172:175], v[172:173], off
	v_add_co_u32_e32 v188, vcc, 0x9c000, v34
	global_load_dwordx4 v[176:179], v[176:177], off
	s_mov_b64 s[0:1], vcc
	v_addc_co_u32_e64 v185, vcc, 0, v35, s[2:3]
	global_load_dwordx4 v[180:183], v[180:181], off
	v_add_co_u32_e32 v192, vcc, 0xa8000, v34
	s_mov_b64 s[2:3], vcc
	global_load_dwordx4 v[184:187], v[184:185], off
	v_addc_co_u32_e64 v189, vcc, 0, v35, s[0:1]
	global_load_dwordx4 v[188:191], v[188:189], off
	v_add_co_u32_e32 v196, vcc, 0xb4000, v34
	v_addc_co_u32_e64 v193, s[0:1], 0, v35, s[2:3]
	global_load_dwordx4 v[192:195], v[192:193], off
	v_addc_co_u32_e32 v197, vcc, 0, v35, vcc
	global_load_dwordx4 v[196:199], v[196:197], off
	s_waitcnt lgkmcnt(3)
	v_mov_b32_e32 v232, v207
	s_waitcnt lgkmcnt(1)
	v_mov_b32_e32 v234, v211
	ds_read_b128 v[216:219], v39 offset:32
	ds_read_b128 v[220:223], v39 offset:48
	ds_read_b128 v[224:227], v39 offset:8224
	ds_read_b128 v[228:231], v39 offset:8240
	v_mov_b32_e32 v236, v203
	s_waitcnt lgkmcnt(4)
	v_mov_b32_e32 v238, v215
	s_waitcnt lgkmcnt(3)
	v_mov_b32_e32 v240, v219
	s_waitcnt lgkmcnt(1)
	v_mov_b32_e32 v242, v227
	v_mov_b32_e32 v244, v223
	s_waitcnt lgkmcnt(0)
	v_mov_b32_e32 v246, v231
	v_add_u32_e32 v39, 64, v39
	v_lshl_add_u64 v[34:35], v[34:35], 0, s[4:5]
	s_add_i32 s11, s11, 32
	s_cmpk_lt_u32 s11, 0xf0
	s_waitcnt vmcnt(31)
	v_pk_fma_f32 v[4:5], v[12:13], v[18:19], v[4:5] op_sel_hi:[1,0,1]
	v_pk_fma_f32 v[2:3], v[10:11], v[18:19], v[2:3] op_sel_hi:[1,0,1]
	v_pk_fma_f32 v[8:9], v[12:13], v[22:23], v[8:9] op_sel_hi:[1,0,1]
	v_pk_fma_f32 v[6:7], v[10:11], v[22:23], v[6:7] op_sel_hi:[1,0,1]
	s_waitcnt vmcnt(30)
	v_pk_fma_f32 v[4:5], v[46:47], v[18:19], v[4:5] op_sel:[0,1,0]
	v_pk_fma_f32 v[2:3], v[44:45], v[18:19], v[2:3] op_sel:[0,1,0]
	v_pk_fma_f32 v[8:9], v[46:47], v[22:23], v[8:9] op_sel:[0,1,0]
	v_pk_fma_f32 v[6:7], v[44:45], v[22:23], v[6:7] op_sel:[0,1,0]
	s_waitcnt vmcnt(29)
	v_pk_fma_f32 v[4:5], v[50:51], v[20:21], v[4:5] op_sel_hi:[1,0,1]
	v_pk_fma_f32 v[2:3], v[48:49], v[20:21], v[2:3] op_sel_hi:[1,0,1]
	v_pk_fma_f32 v[8:9], v[50:51], v[24:25], v[8:9] op_sel_hi:[1,0,1]
	v_pk_fma_f32 v[6:7], v[48:49], v[24:25], v[6:7] op_sel_hi:[1,0,1]
	s_waitcnt vmcnt(28)
	v_pk_fma_f32 v[4:5], v[54:55], v[120:121], v[4:5] op_sel_hi:[1,0,1]
	v_pk_fma_f32 v[2:3], v[52:53], v[120:121], v[2:3] op_sel_hi:[1,0,1]
	v_pk_fma_f32 v[8:9], v[54:55], v[122:123], v[8:9] op_sel_hi:[1,0,1]
	v_pk_fma_f32 v[6:7], v[52:53], v[122:123], v[6:7] op_sel_hi:[1,0,1]
	s_waitcnt vmcnt(27)
	v_pk_fma_f32 v[4:5], v[58:59], v[14:15], v[4:5] op_sel_hi:[1,0,1]
	v_pk_fma_f32 v[2:3], v[56:57], v[14:15], v[2:3] op_sel_hi:[1,0,1]
	v_pk_fma_f32 v[8:9], v[58:59], v[40:41], v[8:9] op_sel_hi:[1,0,1]
	v_pk_fma_f32 v[6:7], v[56:57], v[40:41], v[6:7] op_sel_hi:[1,0,1]
	s_waitcnt vmcnt(26)
	v_pk_fma_f32 v[4:5], v[62:63], v[14:15], v[4:5] op_sel:[0,1,0]
	v_pk_fma_f32 v[2:3], v[60:61], v[14:15], v[2:3] op_sel:[0,1,0]
	v_pk_fma_f32 v[8:9], v[62:63], v[40:41], v[8:9] op_sel:[0,1,0]
	v_pk_fma_f32 v[6:7], v[60:61], v[40:41], v[6:7] op_sel:[0,1,0]
	s_waitcnt vmcnt(25)
	v_pk_fma_f32 v[4:5], v[66:67], v[16:17], v[4:5] op_sel_hi:[1,0,1]
	v_pk_fma_f32 v[2:3], v[64:65], v[16:17], v[2:3] op_sel_hi:[1,0,1]
	v_pk_fma_f32 v[8:9], v[66:67], v[42:43], v[8:9] op_sel_hi:[1,0,1]
	v_pk_fma_f32 v[6:7], v[64:65], v[42:43], v[6:7] op_sel_hi:[1,0,1]
	s_waitcnt vmcnt(24)
	v_pk_fma_f32 v[4:5], v[70:71], v[124:125], v[4:5] op_sel_hi:[1,0,1]
	v_pk_fma_f32 v[2:3], v[68:69], v[124:125], v[2:3] op_sel_hi:[1,0,1]
	v_pk_fma_f32 v[8:9], v[70:71], v[126:127], v[8:9] op_sel_hi:[1,0,1]
	v_pk_fma_f32 v[6:7], v[68:69], v[126:127], v[6:7] op_sel_hi:[1,0,1]
	s_waitcnt vmcnt(23)
	v_pk_fma_f32 v[4:5], v[74:75], v[104:105], v[4:5] op_sel_hi:[1,0,1]
	v_pk_fma_f32 v[2:3], v[72:73], v[104:105], v[2:3] op_sel_hi:[1,0,1]
	v_pk_fma_f32 v[8:9], v[74:75], v[112:113], v[8:9] op_sel_hi:[1,0,1]
	v_pk_fma_f32 v[6:7], v[72:73], v[112:113], v[6:7] op_sel_hi:[1,0,1]
	s_waitcnt vmcnt(22)
	v_pk_fma_f32 v[4:5], v[78:79], v[104:105], v[4:5] op_sel:[0,1,0]
	v_pk_fma_f32 v[2:3], v[76:77], v[104:105], v[2:3] op_sel:[0,1,0]
	v_pk_fma_f32 v[8:9], v[78:79], v[112:113], v[8:9] op_sel:[0,1,0]
	v_pk_fma_f32 v[6:7], v[76:77], v[112:113], v[6:7] op_sel:[0,1,0]
	s_waitcnt vmcnt(21)
	v_pk_fma_f32 v[4:5], v[82:83], v[106:107], v[4:5] op_sel_hi:[1,0,1]
	v_pk_fma_f32 v[2:3], v[80:81], v[106:107], v[2:3] op_sel_hi:[1,0,1]
	v_pk_fma_f32 v[8:9], v[82:83], v[114:115], v[8:9] op_sel_hi:[1,0,1]
	v_pk_fma_f32 v[6:7], v[80:81], v[114:115], v[6:7] op_sel_hi:[1,0,1]
	s_waitcnt vmcnt(20)
	v_pk_fma_f32 v[4:5], v[86:87], v[128:129], v[4:5] op_sel_hi:[1,0,1]
	v_pk_fma_f32 v[2:3], v[84:85], v[128:129], v[2:3] op_sel_hi:[1,0,1]
	v_pk_fma_f32 v[8:9], v[86:87], v[130:131], v[8:9] op_sel_hi:[1,0,1]
	v_pk_fma_f32 v[6:7], v[84:85], v[130:131], v[6:7] op_sel_hi:[1,0,1]
	s_waitcnt vmcnt(19)
	v_pk_fma_f32 v[4:5], v[90:91], v[108:109], v[4:5] op_sel_hi:[1,0,1]
	v_pk_fma_f32 v[2:3], v[88:89], v[108:109], v[2:3] op_sel_hi:[1,0,1]
	v_pk_fma_f32 v[8:9], v[90:91], v[116:117], v[8:9] op_sel_hi:[1,0,1]
	v_pk_fma_f32 v[6:7], v[88:89], v[116:117], v[6:7] op_sel_hi:[1,0,1]
	s_waitcnt vmcnt(18)
	v_pk_fma_f32 v[4:5], v[94:95], v[108:109], v[4:5] op_sel:[0,1,0]
	v_pk_fma_f32 v[2:3], v[92:93], v[108:109], v[2:3] op_sel:[0,1,0]
	v_pk_fma_f32 v[8:9], v[94:95], v[116:117], v[8:9] op_sel:[0,1,0]
	v_pk_fma_f32 v[6:7], v[92:93], v[116:117], v[6:7] op_sel:[0,1,0]
	s_waitcnt vmcnt(17)
	v_pk_fma_f32 v[4:5], v[98:99], v[110:111], v[4:5] op_sel_hi:[1,0,1]
	v_pk_fma_f32 v[2:3], v[96:97], v[110:111], v[2:3] op_sel_hi:[1,0,1]
	v_pk_fma_f32 v[8:9], v[98:99], v[118:119], v[8:9] op_sel_hi:[1,0,1]
	v_pk_fma_f32 v[6:7], v[96:97], v[118:119], v[6:7] op_sel_hi:[1,0,1]
	s_waitcnt vmcnt(16)
	v_pk_fma_f32 v[4:5], v[102:103], v[132:133], v[4:5] op_sel_hi:[1,0,1]
	v_pk_fma_f32 v[2:3], v[100:101], v[132:133], v[2:3] op_sel_hi:[1,0,1]
	v_pk_fma_f32 v[8:9], v[102:103], v[134:135], v[8:9] op_sel_hi:[1,0,1]
	v_pk_fma_f32 v[6:7], v[100:101], v[134:135], v[6:7] op_sel_hi:[1,0,1]
	s_waitcnt vmcnt(15)
	v_pk_fma_f32 v[4:5], v[138:139], v[204:205], v[4:5] op_sel_hi:[1,0,1]
	v_pk_fma_f32 v[2:3], v[136:137], v[204:205], v[2:3] op_sel_hi:[1,0,1]
	v_pk_fma_f32 v[8:9], v[138:139], v[208:209], v[8:9] op_sel_hi:[1,0,1]
	v_pk_fma_f32 v[6:7], v[136:137], v[208:209], v[6:7] op_sel_hi:[1,0,1]
	s_waitcnt vmcnt(14)
	v_pk_fma_f32 v[4:5], v[142:143], v[204:205], v[4:5] op_sel:[0,1,0]
	v_pk_fma_f32 v[2:3], v[140:141], v[204:205], v[2:3] op_sel:[0,1,0]
	v_pk_fma_f32 v[8:9], v[142:143], v[208:209], v[8:9] op_sel:[0,1,0]
	v_pk_fma_f32 v[6:7], v[140:141], v[208:209], v[6:7] op_sel:[0,1,0]
	s_waitcnt vmcnt(13)
	v_pk_fma_f32 v[4:5], v[146:147], v[206:207], v[4:5] op_sel_hi:[1,0,1]
	v_pk_fma_f32 v[2:3], v[144:145], v[206:207], v[2:3] op_sel_hi:[1,0,1]
	v_pk_fma_f32 v[8:9], v[146:147], v[210:211], v[8:9] op_sel_hi:[1,0,1]
	v_pk_fma_f32 v[6:7], v[144:145], v[210:211], v[6:7] op_sel_hi:[1,0,1]
	s_waitcnt vmcnt(12)
	v_pk_fma_f32 v[4:5], v[150:151], v[232:233], v[4:5] op_sel_hi:[1,0,1]
	v_pk_fma_f32 v[2:3], v[148:149], v[232:233], v[2:3] op_sel_hi:[1,0,1]
	v_pk_fma_f32 v[8:9], v[150:151], v[234:235], v[8:9] op_sel_hi:[1,0,1]
	v_pk_fma_f32 v[6:7], v[148:149], v[234:235], v[6:7] op_sel_hi:[1,0,1]
	s_waitcnt vmcnt(11)
	v_pk_fma_f32 v[4:5], v[154:155], v[200:201], v[4:5] op_sel_hi:[1,0,1]
	v_pk_fma_f32 v[2:3], v[152:153], v[200:201], v[2:3] op_sel_hi:[1,0,1]
	v_pk_fma_f32 v[8:9], v[154:155], v[212:213], v[8:9] op_sel_hi:[1,0,1]
	v_pk_fma_f32 v[6:7], v[152:153], v[212:213], v[6:7] op_sel_hi:[1,0,1]
	s_waitcnt vmcnt(10)
	v_pk_fma_f32 v[4:5], v[158:159], v[200:201], v[4:5] op_sel:[0,1,0]
	v_pk_fma_f32 v[2:3], v[156:157], v[200:201], v[2:3] op_sel:[0,1,0]
	v_pk_fma_f32 v[8:9], v[158:159], v[212:213], v[8:9] op_sel:[0,1,0]
	v_pk_fma_f32 v[6:7], v[156:157], v[212:213], v[6:7] op_sel:[0,1,0]
	s_waitcnt vmcnt(9)
	v_pk_fma_f32 v[4:5], v[162:163], v[202:203], v[4:5] op_sel_hi:[1,0,1]
	v_pk_fma_f32 v[2:3], v[160:161], v[202:203], v[2:3] op_sel_hi:[1,0,1]
	v_pk_fma_f32 v[8:9], v[162:163], v[214:215], v[8:9] op_sel_hi:[1,0,1]
	v_pk_fma_f32 v[6:7], v[160:161], v[214:215], v[6:7] op_sel_hi:[1,0,1]
	s_waitcnt vmcnt(8)
	v_pk_fma_f32 v[4:5], v[166:167], v[236:237], v[4:5] op_sel_hi:[1,0,1]
	v_pk_fma_f32 v[2:3], v[164:165], v[236:237], v[2:3] op_sel_hi:[1,0,1]
	v_pk_fma_f32 v[8:9], v[166:167], v[238:239], v[8:9] op_sel_hi:[1,0,1]
	v_pk_fma_f32 v[6:7], v[164:165], v[238:239], v[6:7] op_sel_hi:[1,0,1]
	s_waitcnt vmcnt(7)
	v_pk_fma_f32 v[4:5], v[170:171], v[216:217], v[4:5] op_sel_hi:[1,0,1]
	v_pk_fma_f32 v[2:3], v[168:169], v[216:217], v[2:3] op_sel_hi:[1,0,1]
	v_pk_fma_f32 v[8:9], v[170:171], v[224:225], v[8:9] op_sel_hi:[1,0,1]
	v_pk_fma_f32 v[6:7], v[168:169], v[224:225], v[6:7] op_sel_hi:[1,0,1]
	s_waitcnt vmcnt(6)
	v_pk_fma_f32 v[4:5], v[174:175], v[216:217], v[4:5] op_sel:[0,1,0]
	v_pk_fma_f32 v[2:3], v[172:173], v[216:217], v[2:3] op_sel:[0,1,0]
	v_pk_fma_f32 v[8:9], v[174:175], v[224:225], v[8:9] op_sel:[0,1,0]
	v_pk_fma_f32 v[6:7], v[172:173], v[224:225], v[6:7] op_sel:[0,1,0]
	s_waitcnt vmcnt(5)
	v_pk_fma_f32 v[4:5], v[178:179], v[218:219], v[4:5] op_sel_hi:[1,0,1]
	v_pk_fma_f32 v[2:3], v[176:177], v[218:219], v[2:3] op_sel_hi:[1,0,1]
	v_pk_fma_f32 v[8:9], v[178:179], v[226:227], v[8:9] op_sel_hi:[1,0,1]
	v_pk_fma_f32 v[6:7], v[176:177], v[226:227], v[6:7] op_sel_hi:[1,0,1]
	s_waitcnt vmcnt(4)
	v_pk_fma_f32 v[4:5], v[182:183], v[240:241], v[4:5] op_sel_hi:[1,0,1]
	v_pk_fma_f32 v[2:3], v[180:181], v[240:241], v[2:3] op_sel_hi:[1,0,1]
	v_pk_fma_f32 v[8:9], v[182:183], v[242:243], v[8:9] op_sel_hi:[1,0,1]
	v_pk_fma_f32 v[6:7], v[180:181], v[242:243], v[6:7] op_sel_hi:[1,0,1]
	s_waitcnt vmcnt(3)
	v_pk_fma_f32 v[4:5], v[186:187], v[220:221], v[4:5] op_sel_hi:[1,0,1]
	v_pk_fma_f32 v[2:3], v[184:185], v[220:221], v[2:3] op_sel_hi:[1,0,1]
	v_pk_fma_f32 v[8:9], v[186:187], v[228:229], v[8:9] op_sel_hi:[1,0,1]
	v_pk_fma_f32 v[6:7], v[184:185], v[228:229], v[6:7] op_sel_hi:[1,0,1]
	s_waitcnt vmcnt(2)
	v_pk_fma_f32 v[4:5], v[190:191], v[220:221], v[4:5] op_sel:[0,1,0]
	v_pk_fma_f32 v[2:3], v[188:189], v[220:221], v[2:3] op_sel:[0,1,0]
	v_pk_fma_f32 v[8:9], v[190:191], v[228:229], v[8:9] op_sel:[0,1,0]
	v_pk_fma_f32 v[6:7], v[188:189], v[228:229], v[6:7] op_sel:[0,1,0]
	s_waitcnt vmcnt(1)
	v_pk_fma_f32 v[4:5], v[194:195], v[222:223], v[4:5] op_sel_hi:[1,0,1]
	v_pk_fma_f32 v[2:3], v[192:193], v[222:223], v[2:3] op_sel_hi:[1,0,1]
	v_pk_fma_f32 v[8:9], v[194:195], v[230:231], v[8:9] op_sel_hi:[1,0,1]
	v_pk_fma_f32 v[6:7], v[192:193], v[230:231], v[6:7] op_sel_hi:[1,0,1]
	s_waitcnt vmcnt(0)
	v_pk_fma_f32 v[4:5], v[198:199], v[244:245], v[4:5] op_sel_hi:[1,0,1]
	v_pk_fma_f32 v[2:3], v[196:197], v[244:245], v[2:3] op_sel_hi:[1,0,1]
	v_pk_fma_f32 v[8:9], v[198:199], v[246:247], v[8:9] op_sel_hi:[1,0,1]
	v_pk_fma_f32 v[6:7], v[196:197], v[246:247], v[6:7] op_sel_hi:[1,0,1]
	s_cbranch_scc1 .LBB0_21
	v_readlane_b32 s12, v254, 2
	ds_write_b128 v27, v[2:5]
	ds_write_b128 v27, v[6:9] offset:1024
	v_or_b32_sdwa v2, s10, v0 dst_sel:DWORD dst_unused:UNUSED_PAD src0_sel:DWORD src1_sel:BYTE_0
	s_mul_i32 s0, s7, 0xc000
	v_readlane_b32 s18, v254, 8
	v_ashrrev_i32_e32 v3, 31, v2
	s_mul_hi_i32 s1, s7, 0xc000
	v_readlane_b32 s19, v254, 9
	s_add_u32 s0, s18, s0
	s_addc_u32 s1, s19, s1
	v_lshlrev_b64 v[2:3], 2, v[2:3]
	v_lshl_add_u64 v[4:5], s[0:1], 0, v[2:3]
	s_waitcnt lgkmcnt(0)
	s_waitcnt lgkmcnt(0)
	s_barrier
	global_load_dword v14, v[4:5], off
	ds_read2st64_b32 v[6:7], v36 offset1:8
	ds_read2st64_b32 v[8:9], v36 offset0:16 offset1:24
	ds_read2st64_b32 v[10:11], v36 offset0:32 offset1:40
	ds_read2st64_b32 v[12:13], v36 offset0:48 offset1:56
	v_mad_i64_i32 v[4:5], s[0:1], s7, v38, v[32:33]
	v_lshl_add_u64 v[2:3], v[4:5], 0, v[2:3]
	s_waitcnt lgkmcnt(3)
	v_add_f32_e32 v4, 0, v6
	v_add_f32_e32 v4, v4, v7
	s_waitcnt lgkmcnt(2)
	v_add_f32_e32 v4, v4, v8
	v_add_f32_e32 v4, v4, v9
	s_waitcnt lgkmcnt(1)
	v_add_f32_e32 v4, v4, v10
	v_add_f32_e32 v4, v4, v11
	s_waitcnt lgkmcnt(0)
	v_add_f32_e32 v4, v4, v12
	s_add_i32 s6, s6, s9
	v_add_f32_e32 v4, v4, v13
	s_cmpk_gt_i32 s6, 0x5f
	v_readlane_b32 s13, v254, 3
	v_readlane_b32 s14, v254, 4
	v_readlane_b32 s15, v254, 5
	v_readlane_b32 s16, v254, 6
	v_readlane_b32 s17, v254, 7
	v_readlane_b32 s20, v254, 10
	v_readlane_b32 s21, v254, 11
	v_readlane_b32 s22, v254, 12
	v_readlane_b32 s23, v254, 13
	v_readlane_b32 s24, v254, 14
	v_readlane_b32 s25, v254, 15
	v_readlane_b32 s26, v254, 16
	v_readlane_b32 s27, v254, 17
	s_waitcnt vmcnt(0)
	v_add_f32_e32 v4, v4, v14
	global_store_dword v[2:3], v4, off
	s_barrier
	s_cbranch_scc0 .LBB0_20
	v_mov_b32_e32 v2, v26
